# static s_setprio 1 for waves 4-7 during the attention and spatial-gating phases (reset to 0 at phase end)
# speedup vs baseline: 1.0288x; 1.0003x over previous
.LBB0_531:
	s_cmp_lt_i32 s28, 4
	s_cselect_b64 s[84:85], -1, 0
	s_and_b64 s[0:1], s[84:85], s[4:5]
	s_andn2_b64 vcc, exec, s[0:1]
	s_cbranch_vccnz .LBB0_561
	s_getreg_b32 s0, hwreg(HW_REG_HW_ID, 0, 6)
	s_lshl_b32 s0, s0, 2
	s_and_b32 s0, s0, 0xfc
	s_add_i32 s0, s0, 0
	s_add_i32 s0, s0, 0x25c00
	v_mov_b32_e32 v0, s0
	ds_read_b32 v0, v0
	s_cmpk_gt_i32 s2, 0x1ff
	s_waitcnt lgkmcnt(0)
	v_readfirstlane_b32 s0, v0
	v_mbcnt_lo_u32_b32 v0, -1, 0
	v_mbcnt_hi_u32_b32 v0, -1, v0
	s_nop 1
	v_lshl_add_u32 v2, s0, 6, v0
	s_nop 0
	v_readfirstlane_b32 s16, v2
	s_cbranch_scc1 .LBB0_560
	s_cmp_lt_u32 s16, 0x100
	s_cbranch_scc1 .Lattn_prio_set
	s_setprio 1
.Lattn_prio_set:
	v_readlane_b32 s4, v249, 55
	v_readlane_b32 s10, v249, 61
	v_readlane_b32 s11, v249, 62
	s_add_u32 s86, s10, 0x14500000
	s_addc_u32 s87, s11, 0
	s_add_u32 s88, s10, 0x14d00000
	s_addc_u32 s89, s11, 0
	s_ashr_i32 s0, s2, 8
	s_bfe_u32 s3, s2, 0x60002
	s_ashr_i32 s1, s0, 31
	s_lshl_b64 s[10:11], s[0:1], 13
	s_lshl_b32 s0, s3, 7
	s_or_b32 s10, s10, s0
	s_cmp_lg_u32 s3, 0
	s_cselect_b64 s[14:15], -1, 0
	s_lshl_b32 s0, s2, 7
	s_and_b32 s0, s0, 0x180
	s_add_u32 s12, s86, s0
	v_mov_b32_e32 v80, 0
	v_readlane_b32 s8, v249, 59
	s_addc_u32 s13, s87, 0
	v_ashrrev_i32_e32 v112, 3, v2
	s_movk_i32 s3, 0x7f
	v_mov_b32_e32 v82, v80
	v_mov_b32_e32 v83, v80
	v_readlane_b32 s6, v249, 57
	v_readlane_b32 s7, v249, 58
	v_readlane_b32 s9, v249, 60
	s_add_u32 s8, s88, s0
	v_cmp_lt_i32_e64 s[0:1], s3, v112
	v_mov_b32_e32 v81, v80
	v_mov_b64_e32 v[86:87], v[82:83]
	v_mov_b64_e32 v[90:91], v[82:83]
	v_readlane_b32 s5, v249, 56
	s_addc_u32 s9, s89, 0
	s_or_b64 s[6:7], s[14:15], s[0:1]
	v_ashrrev_i32_e32 v113, 31, v112
	v_lshlrev_b32_e32 v3, 4, v2
	v_mov_b64_e32 v[84:85], v[80:81]
	v_mov_b64_e32 v[88:89], v[80:81]
	s_and_saveexec_b64 s[4:5], s[6:7]
	s_cbranch_execz .LBB0_535
	v_lshl_add_u64 v[0:1], s[10:11], 0, v[112:113]
	s_mov_b32 s6, 0xffff0000
	v_lshlrev_b64 v[0:1], 9, v[0:1]
	s_mov_b32 s7, -1
	v_lshl_add_u64 v[0:1], v[0:1], 0, s[6:7]
	v_lshl_add_u64 v[4:5], s[12:13], 0, v[0:1]
	v_and_b32_e32 v6, 0x70, v3
	v_mov_b32_e32 v7, v80
	v_lshl_add_u64 v[4:5], v[4:5], 0, v[6:7]
	v_lshl_add_u64 v[0:1], s[8:9], 0, v[0:1]
	v_lshl_add_u64 v[0:1], v[0:1], 0, v[6:7]
	global_load_dwordx4 v[88:91], v[4:5], off
	global_load_dwordx4 v[84:87], v[0:1], off

.LBB0_560:
	s_setprio 0
	v_readlane_b32 s72, v249, 55
	v_readlane_b32 s73, v249, 56
	v_readlane_b32 s74, v249, 57
	v_readlane_b32 s75, v249, 58
	v_readlane_b32 s76, v249, 59
	v_readlane_b32 s77, v249, 60
	v_readlane_b32 s78, v249, 61
	v_readlane_b32 s79, v249, 62
	s_barrier

.LBB0_1958:
	s_cmp_lt_i32 s48, 11
	s_cselect_b64 s[10:11], -1, 0
	s_and_b64 s[0:1], s[10:11], s[4:5]
	s_andn2_b64 vcc, exec, s[0:1]
	s_cbranch_vccnz .LBB0_1973
	s_getreg_b32 s0, hwreg(HW_REG_HW_ID, 0, 6)
	s_lshl_b32 s0, s0, 2
	s_and_b32 s0, s0, 0xfc
	s_add_i32 s0, s0, 0
	s_add_i32 s0, s0, 0x25c00
	v_mov_b32_e32 v0, s0
	ds_read_b32 v0, v0
	s_cmpk_gt_i32 s2, 0x3ff
	s_waitcnt lgkmcnt(0)
	v_readfirstlane_b32 s0, v0
	v_mbcnt_lo_u32_b32 v0, -1, 0
	v_mbcnt_hi_u32_b32 v0, -1, v0
	s_nop 1
	v_lshl_add_u32 v158, s0, 6, v0
	s_nop 0
	v_readfirstlane_b32 s30, v158
	s_cbranch_scc1 .LBB0_1972
	s_cmp_lt_u32 s30, 0x100
	s_cbranch_scc1 .Lsgu_prio_set
	s_setprio 1
.Lsgu_prio_set:
	s_add_u32 s12, s78, 0x12500000
	s_addc_u32 s13, s79, 0
	s_add_u32 s14, s78, 0x16500000
	s_addc_u32 s15, s79, 0
	s_add_u32 s3, s78, 0x1a500000
	s_addc_u32 s34, s79, 0
	s_lshl_b32 s0, s2, 8
	s_and_b32 s4, s0, 0x700
	s_ashr_i32 s0, s2, 3
	s_ashr_i32 s1, s0, 31
	v_ashrrev_i32_e32 v130, 5, v158
	s_lshl_b64 s[0:1], s[0:1], 7
	v_and_b32_e32 v71, 31, v158
	v_ashrrev_i32_e32 v131, 31, v130
	v_lshlrev_b32_e32 v159, 3, v71
	v_lshl_add_u64 v[0:1], s[0:1], 0, v[130:131]
	v_or_b32_e32 v2, s4, v159
	v_lshlrev_b64 v[14:15], 12, v[0:1]
	v_lshl_or_b32 v14, v2, 1, v14
	s_mov_b64 s[16:17], 0x10000
	v_lshl_add_u64 v[2:3], s[14:15], 0, v[14:15]
	v_lshl_add_u64 v[4:5], v[14:15], 0, s[16:17]
	s_mov_b64 s[18:19], 0x20000
	v_ashrrev_i32_e32 v128, 2, v158
	v_lshl_add_u64 v[6:7], s[14:15], 0, v[4:5]
	global_load_dwordx4 v[16:19], v[2:3], off nt
	global_load_dwordx4 v[20:23], v[6:7], off nt
	v_lshl_add_u64 v[2:3], s[12:13], 0, v[4:5]
	v_lshl_add_u64 v[4:5], v[14:15], 0, s[18:19]
	s_mov_b64 s[20:21], 0x30000
	v_lshl_add_u64 v[6:7], s[14:15], 0, v[4:5]
	v_lshl_add_u64 v[8:9], v[14:15], 0, s[20:21]
	s_mov_b64 s[22:23], 0x40000
	s_mov_b64 s[24:25], 0x50000
	v_ashrrev_i32_e32 v129, 31, v128
	s_add_u32 s6, s78, 0x600000
	v_lshl_add_u64 v[10:11], s[14:15], 0, v[8:9]
	global_load_dwordx4 v[24:27], v[6:7], off nt
	global_load_dwordx4 v[28:31], v[10:11], off nt
	v_lshl_add_u64 v[6:7], s[12:13], 0, v[8:9]
	v_lshl_add_u64 v[8:9], v[14:15], 0, s[22:23]
	v_lshl_add_u64 v[12:13], v[14:15], 0, s[24:25]
	s_waitcnt vmcnt(0)
	v_lshl_add_u64 v[48:49], s[0:1], 0, v[128:129]
	s_addc_u32 s7, s79, 0
	v_and_b32_e32 v64, 3, v158
	v_lshl_add_u64 v[10:11], s[14:15], 0, v[8:9]
	v_lshl_add_u64 v[36:37], s[14:15], 0, v[12:13]
	s_mov_b64 s[26:27], 0x60000
	s_mov_b64 s[28:29], 0x70000
	v_lshlrev_b64 v[48:49], 8, v[48:49]
	v_lshl_add_u64 v[0:1], s[12:13], 0, v[14:15]
	global_load_dwordx4 v[32:35], v[10:11], off nt
	s_nop 0
	global_load_dwordx4 v[36:39], v[36:37], off nt
	v_lshl_add_u64 v[10:11], s[12:13], 0, v[12:13]
	v_lshl_add_u64 v[12:13], v[14:15], 0, s[26:27]
	v_lshl_add_u64 v[14:15], v[14:15], 0, s[28:29]
	v_lshl_add_u64 v[48:49], s[6:7], 0, v[48:49]
	v_lshlrev_b32_e32 v132, 6, v64
	v_mov_b32_e32 v133, 0
	v_lshl_add_u64 v[40:41], s[14:15], 0, v[12:13]
	v_lshl_add_u64 v[44:45], s[14:15], 0, v[14:15]
	v_lshl_add_u64 v[60:61], v[48:49], 0, v[132:133]
	global_load_dwordx4 v[40:43], v[40:41], off nt
	s_nop 0
	global_load_dwordx4 v[44:47], v[44:45], off nt
	s_nop 0
	global_load_dwordx4 v[48:51], v[60:61], off offset:48
	global_load_dwordx4 v[52:55], v[60:61], off offset:32
	global_load_dwordx4 v[56:59], v[60:61], off offset:16
	s_nop 0
	global_load_dwordx4 v[60:63], v[60:61], off
	v_mbcnt_lo_u32_b32 v65, -1, 0
	v_mbcnt_hi_u32_b32 v65, -1, v65
	v_and_b32_e32 v67, 64, v65
	v_xor_b32_e32 v66, 1, v65
	v_add_u32_e32 v67, 64, v67
	v_cmp_lt_i32_e32 vcc, v66, v67
	v_cmp_eq_u32_e64 s[0:1], 0, v64
	v_lshlrev_b32_e32 v64, 4, v158
	v_cndmask_b32_e32 v66, v65, v66, vcc
	v_lshlrev_b32_e32 v160, 2, v66
	v_xor_b32_e32 v66, 2, v65
	v_cmp_lt_i32_e32 vcc, v66, v67
	v_and_b32_e32 v64, 0xf0, v64
	v_lshlrev_b32_e32 v70, 2, v158
	v_cndmask_b32_e32 v65, v65, v66, vcc
	v_lshlrev_b32_e32 v161, 2, v65
	v_mov_b32_e32 v65, v133
	v_lshl_add_u64 v[66:67], s[78:79], 0, v[64:65]
	s_mov_b64 s[36:37], 0x500000
	v_lshl_add_u64 v[136:137], s[6:7], 0, v[132:133]
	s_ashr_i32 s7, s30, 1
	v_bfe_u32 v69, v158, 5, 1
	v_lshl_add_u64 v[134:135], v[66:67], 0, s[36:37]
	v_add_u32_e32 v79, 0, v64
	v_bfe_u32 v64, v158, 2, 2
	s_andn2_b32 s7, s7, 31
	v_and_b32_e32 v65, 16, v158
	v_and_b32_e32 v66, 12, v70
	v_lshl_or_b32 v64, v69, 3, v64
	v_or3_b32 v65, v65, v66, s7
	v_mul_u32_u24_e32 v64, 0x240, v64
	v_lshlrev_b32_e32 v65, 1, v65
	s_add_i32 s31, 0, 0x1ac00
	v_add3_u32 v164, 0, v64, v65
	v_lshlrev_b32_e32 v65, 4, v69
	s_movk_i32 s6, 0x240
	v_add_u32_e32 v81, 0, v65
	v_add_u32_e32 v180, s31, v65
	v_lshl_or_b32 v65, v69, 2, 1
	v_mov_b32_e32 v67, 0x1440
	v_mad_u32_u24 v90, v65, s6, v67
	v_mov_b32_e32 v67, 0x2880
	v_mad_u32_u24 v91, v65, s6, v67
	v_mov_b32_e32 v67, 0x45c0
	v_add_u32_e32 v64, 0x200, v158
	v_mad_u32_u24 v92, v65, s6, v67
	v_mov_b32_e32 v67, 0x5a00
	v_ashrrev_i32_e32 v167, 4, v64
	v_add_u32_e32 v64, 0x400, v158
	v_mad_u32_u24 v93, v65, s6, v67
	v_mov_b32_e32 v67, 0x6e40
	v_ashrrev_i32_e32 v168, 4, v64
	v_add_u32_e32 v64, 0x600, v158
	v_mad_u32_u24 v94, v65, s6, v67
	v_mov_b32_e32 v67, 0x8280
	v_lshl_add_u32 v68, v71, 1, 0
	v_ashrrev_i32_e32 v169, 4, v64
	v_add_u32_e32 v64, 16, v130
	v_mad_u32_u24 v95, v65, s6, v67
	v_mov_b32_e32 v67, 0x9fc0
	v_lshlrev_b32_e32 v78, 3, v128
	v_add_u32_e32 v162, s31, v70
	v_mad_u32_u24 v163, v71, 14, v68
	v_lshl_add_u32 v80, s7, 1, v68
	v_ashrrev_i32_e32 v166, 4, v158
	s_movk_i32 s7, 0x110
	v_mul_lo_u32 v171, v130, s6
	v_add_u32_e32 v66, 32, v130
	v_add_u32_e32 v68, 48, v130
	v_add_u32_e32 v70, 64, v130
	v_add_u32_e32 v72, 0x50, v130
	v_add_u32_e32 v74, 0x60, v130
	v_add_u32_e32 v76, 0x70, v130
	v_mul_u32_u24_e32 v89, 0x240, v65
	v_mad_u32_u24 v96, v65, s6, v67
	v_ashrrev_i32_e32 v65, 31, v64
	s_movk_i32 s4, 0x80
	v_mul_lo_u32 v82, v166, s7
	v_mul_lo_u32 v83, v167, s7
	v_mul_lo_u32 v84, v168, s7
	v_mul_lo_u32 v85, v169, s7
	v_lshlrev_b32_e32 v172, 3, v64
	v_add_u32_e32 v86, 0x9000, v171
	v_mul_u32_u24_e32 v87, 0x110, v71
	v_mul_u32_u24_e32 v88, 0x900, v69
	v_lshlrev_b64 v[140:141], 11, v[64:65]
	v_ashrrev_i32_e32 v67, 31, v66
	v_ashrrev_i32_e32 v69, 31, v68
	v_ashrrev_i32_e32 v71, 31, v70
	v_ashrrev_i32_e32 v73, 31, v72
	v_ashrrev_i32_e32 v75, 31, v74
	v_ashrrev_i32_e32 v77, 31, v76
	s_add_i32 s6, s2, s33
	v_add_u32_e32 v64, 0, v78
	v_lshl_add_u64 v[4:5], s[12:13], 0, v[4:5]
	v_lshl_add_u64 v[8:9], s[12:13], 0, v[8:9]
	v_lshl_add_u64 v[12:13], s[12:13], 0, v[12:13]
	v_lshl_add_u64 v[14:15], s[12:13], 0, v[14:15]
	s_mov_b32 s35, -1
	v_cmp_gt_i32_e64 s[4:5], s4, v158
	v_add_u32_e32 v165, 0x8800, v164
	v_lshlrev_b32_e32 v170, 3, v130
	v_lshlrev_b32_e32 v173, 3, v66
	v_lshlrev_b32_e32 v174, 3, v68
	v_lshlrev_b32_e32 v175, 3, v70
	v_lshlrev_b32_e32 v176, 3, v72
	v_lshlrev_b32_e32 v177, 3, v74
	v_lshlrev_b32_e32 v178, 3, v76
	v_add_u32_e32 v179, 0x18d00, v164
	v_add_u32_e32 v181, 32, v180
	v_add_u32_e32 v182, 64, v180
	v_add_u32_e32 v183, 0x60, v180
	v_add_u32_e32 v184, 0x80, v180
	v_add_u32_e32 v185, 0xa0, v180
	v_add_u32_e32 v186, 0xc0, v180
	v_add_u32_e32 v187, 0xe0, v180
	v_add_u32_e32 v188, 0x100, v180
	v_add_u32_e32 v189, 0x120, v180
	v_add_u32_e32 v190, 0x140, v180
	v_add_u32_e32 v191, 0x160, v180
	v_add_u32_e32 v192, 0x180, v180
	v_add_u32_e32 v193, 0x1a0, v180
	v_add_u32_e32 v194, 0x1c0, v180
	v_add_u32_e32 v195, 0x1e0, v180
	v_lshlrev_b64 v[138:139], 11, v[130:131]
	v_lshlrev_b64 v[142:143], 11, v[66:67]
	v_lshlrev_b64 v[144:145], 11, v[68:69]
	v_lshlrev_b64 v[146:147], 11, v[70:71]
	v_lshlrev_b64 v[148:149], 11, v[72:73]
	v_lshlrev_b64 v[150:151], 11, v[74:75]
	v_lshlrev_b64 v[152:153], 11, v[76:77]
	s_lshl_b32 s36, s6, 8
	s_lshl_b32 s37, s33, 8
	s_mov_b32 s38, 0x3a000000
	v_add_u32_e32 v196, 0x1a800, v64
	s_mov_b32 s39, 0xf800000
	v_mov_b32_e32 v197, 0x260
	v_add_u32_e32 v198, v79, v82
	v_add_u32_e32 v199, v79, v83
	v_add_u32_e32 v200, v79, v84
	v_add_u32_e32 v201, v79, v85
	v_add_u32_e32 v202, v81, v87
	v_add_u32_e32 v203, v80, v88
	v_add_u32_e32 v204, v80, v89
	v_add_u32_e32 v205, v80, v90
	v_add_u32_e32 v206, v80, v91
	v_add_u32_e32 v207, v80, v92
	v_add_u32_e32 v208, v80, v93
	v_add_u32_e32 v209, v80, v94
	v_add_u32_e32 v210, v80, v95
	v_add_u32_e32 v211, v80, v96
	s_mov_b32 s40, 0xc3e00000
	v_add_u32_e32 v212, v163, v86
	v_mov_b32_e32 v213, 0x43e00000
	s_mov_b32 s42, s2
	s_branch .LBB0_1962

.LBB0_1972:
	s_setprio 0
	s_waitcnt vmcnt(0)
	s_barrier
